# v99 + lever 7 (instruction selection): the zero-initialising v_pk_add_f32 of 16 softmax row-sum chains folded into the chain's first add (exact)
# speedup vs baseline: 1.0098x; 1.0098x over previous
.LBB0_496:
	s_add_i32 s63, s63, 2
	v_pk_add_f32 v[64:65], v[64:65], v[80:81]
	s_add_u32 s74, s74, 0xd0000
	v_pk_add_f32 v[64:65], v[66:67], v[64:65]
	s_addc_u32 s75, s75, 0
	v_pk_add_f32 v[64:65], v[82:83], v[64:65]
	s_and_b64 vcc, exec, s[2:3]
	v_pk_add_f32 v[64:65], v[68:69], v[64:65]
	s_waitcnt lgkmcnt(0)
	v_pk_add_f32 v[64:65], v[84:85], v[64:65]
	s_barrier
	v_pk_add_f32 v[64:65], v[70:71], v[64:65]
	s_nop 0
	v_pk_add_f32 v[64:65], v[86:87], v[64:65]
	s_nop 0
	v_pk_add_f32 v[64:65], v[72:73], v[64:65]
	s_nop 0
	v_pk_add_f32 v[64:65], v[88:89], v[64:65]
	s_nop 0
	v_pk_add_f32 v[64:65], v[74:75], v[64:65]
	s_nop 0
	v_pk_add_f32 v[64:65], v[90:91], v[64:65]
	s_nop 0
	v_pk_add_f32 v[64:65], v[76:77], v[64:65]
	s_nop 0
	v_pk_add_f32 v[64:65], v[92:93], v[64:65]
	s_nop 0
	v_pk_add_f32 v[64:65], v[78:79], v[64:65]
	s_nop 0
	v_pk_add_f32 v[64:65], v[94:95], v[64:65]
	s_nop 0
	v_add_f32_e32 v64, v64, v65
	v_add_f32_e32 v66, v215, v64
	s_nop 0
	v_pk_add_f32 v[64:65], v[96:97], v[144:145]
	s_nop 0
	v_pk_add_f32 v[64:65], v[98:99], v[64:65]
	s_nop 0
	v_pk_add_f32 v[64:65], v[146:147], v[64:65]
	s_nop 0
	v_pk_add_f32 v[64:65], v[100:101], v[64:65]
	s_nop 0
	v_pk_add_f32 v[64:65], v[148:149], v[64:65]
	s_nop 0
	v_pk_add_f32 v[64:65], v[102:103], v[64:65]
	s_nop 0
	v_pk_add_f32 v[64:65], v[150:151], v[64:65]
	s_nop 0
	v_pk_add_f32 v[64:65], v[104:105], v[64:65]
	s_nop 0
	v_pk_add_f32 v[64:65], v[152:153], v[64:65]
	s_nop 0
	v_pk_add_f32 v[64:65], v[106:107], v[64:65]
	s_nop 0
	v_pk_add_f32 v[64:65], v[154:155], v[64:65]
	s_nop 0
	v_pk_add_f32 v[64:65], v[108:109], v[64:65]
	s_nop 0
	v_pk_add_f32 v[64:65], v[156:157], v[64:65]
	s_nop 0
	v_pk_add_f32 v[64:65], v[110:111], v[64:65]
	s_nop 0
	v_pk_add_f32 v[64:65], v[158:159], v[64:65]
	s_nop 0
	v_add_f32_e32 v64, v64, v65
	v_add_f32_e32 v215, v66, v64
	s_cbranch_vccnz .LBB0_519

.LBB0_522:
	s_add_i32 s63, s63, 2
	v_pk_add_f32 v[64:65], v[64:65], v[80:81]
	s_add_u32 s74, s74, 0xd0000
	v_pk_add_f32 v[64:65], v[66:67], v[64:65]
	s_addc_u32 s75, s75, 0
	v_pk_add_f32 v[64:65], v[82:83], v[64:65]
	s_and_b64 vcc, exec, s[2:3]
	v_pk_add_f32 v[64:65], v[68:69], v[64:65]
	s_waitcnt lgkmcnt(0)
	v_pk_add_f32 v[64:65], v[84:85], v[64:65]
	s_barrier
	v_pk_add_f32 v[64:65], v[70:71], v[64:65]
	s_nop 0
	v_pk_add_f32 v[64:65], v[86:87], v[64:65]
	s_nop 0
	v_pk_add_f32 v[64:65], v[72:73], v[64:65]
	s_nop 0
	v_pk_add_f32 v[64:65], v[88:89], v[64:65]
	s_nop 0
	v_pk_add_f32 v[64:65], v[74:75], v[64:65]
	s_nop 0
	v_pk_add_f32 v[64:65], v[90:91], v[64:65]
	s_nop 0
	v_pk_add_f32 v[64:65], v[76:77], v[64:65]
	s_nop 0
	v_pk_add_f32 v[64:65], v[92:93], v[64:65]
	s_nop 0
	v_pk_add_f32 v[64:65], v[78:79], v[64:65]
	s_nop 0
	v_pk_add_f32 v[64:65], v[94:95], v[64:65]
	s_nop 0
	v_add_f32_e32 v64, v64, v65
	v_add_f32_e32 v66, v215, v64
	s_nop 0
	v_pk_add_f32 v[64:65], v[96:97], v[112:113]
	s_nop 0
	v_pk_add_f32 v[64:65], v[98:99], v[64:65]
	s_nop 0
	v_pk_add_f32 v[64:65], v[114:115], v[64:65]
	s_nop 0
	v_pk_add_f32 v[64:65], v[100:101], v[64:65]
	s_nop 0
	v_pk_add_f32 v[64:65], v[116:117], v[64:65]
	s_nop 0
	v_pk_add_f32 v[64:65], v[102:103], v[64:65]
	s_nop 0
	v_pk_add_f32 v[64:65], v[118:119], v[64:65]
	s_nop 0
	v_pk_add_f32 v[64:65], v[104:105], v[64:65]
	s_nop 0
	v_pk_add_f32 v[64:65], v[120:121], v[64:65]
	s_nop 0
	v_pk_add_f32 v[64:65], v[106:107], v[64:65]
	s_nop 0
	v_pk_add_f32 v[64:65], v[122:123], v[64:65]
	s_nop 0
	v_pk_add_f32 v[64:65], v[108:109], v[64:65]
	s_nop 0
	v_pk_add_f32 v[64:65], v[124:125], v[64:65]
	s_nop 0
	v_pk_add_f32 v[64:65], v[110:111], v[64:65]
	s_nop 0
	v_pk_add_f32 v[64:65], v[126:127], v[64:65]
	s_nop 0
	v_add_f32_e32 v64, v64, v65
	v_add_f32_e32 v215, v66, v64
	s_cbranch_vccnz .LBB0_543

.LBB0_547:
	s_add_i32 s10, s10, 2
	v_pk_add_f32 v[64:65], v[64:65], v[80:81]
	s_add_u32 s90, s90, 0xd0000
	v_pk_add_f32 v[64:65], v[66:67], v[64:65]
	s_addc_u32 s91, s91, 0
	v_pk_add_f32 v[64:65], v[82:83], v[64:65]
	s_and_b64 vcc, exec, s[2:3]
	v_pk_add_f32 v[64:65], v[68:69], v[64:65]
	s_waitcnt lgkmcnt(0)
	v_pk_add_f32 v[64:65], v[84:85], v[64:65]
	s_barrier
	v_pk_add_f32 v[64:65], v[70:71], v[64:65]
	s_nop 0
	v_pk_add_f32 v[64:65], v[86:87], v[64:65]
	s_nop 0
	v_pk_add_f32 v[64:65], v[72:73], v[64:65]
	s_nop 0
	v_pk_add_f32 v[64:65], v[88:89], v[64:65]
	s_nop 0
	v_pk_add_f32 v[64:65], v[74:75], v[64:65]
	s_nop 0
	v_pk_add_f32 v[64:65], v[90:91], v[64:65]
	s_nop 0
	v_pk_add_f32 v[64:65], v[76:77], v[64:65]
	s_nop 0
	v_pk_add_f32 v[64:65], v[92:93], v[64:65]
	s_nop 0
	v_pk_add_f32 v[64:65], v[78:79], v[64:65]
	s_nop 0
	v_pk_add_f32 v[64:65], v[94:95], v[64:65]
	s_nop 0
	v_add_f32_e32 v64, v64, v65
	v_add_f32_e32 v66, v215, v64
	s_nop 0
	v_pk_add_f32 v[64:65], v[96:97], v[144:145]
	s_nop 0
	v_pk_add_f32 v[64:65], v[98:99], v[64:65]
	s_nop 0
	v_pk_add_f32 v[64:65], v[146:147], v[64:65]
	s_nop 0
	v_pk_add_f32 v[64:65], v[100:101], v[64:65]
	s_nop 0
	v_pk_add_f32 v[64:65], v[148:149], v[64:65]
	s_nop 0
	v_pk_add_f32 v[64:65], v[102:103], v[64:65]
	s_nop 0
	v_pk_add_f32 v[64:65], v[150:151], v[64:65]
	s_nop 0
	v_pk_add_f32 v[64:65], v[104:105], v[64:65]
	s_nop 0
	v_pk_add_f32 v[64:65], v[152:153], v[64:65]
	s_nop 0
	v_pk_add_f32 v[64:65], v[106:107], v[64:65]
	s_nop 0
	v_pk_add_f32 v[64:65], v[154:155], v[64:65]
	s_nop 0
	v_pk_add_f32 v[64:65], v[108:109], v[64:65]
	s_nop 0
	v_pk_add_f32 v[64:65], v[156:157], v[64:65]
	s_nop 0
	v_pk_add_f32 v[64:65], v[110:111], v[64:65]
	s_nop 0
	v_pk_add_f32 v[64:65], v[158:159], v[64:65]
	s_nop 0
	v_add_f32_e32 v64, v64, v65
	v_add_f32_e32 v215, v66, v64
	s_cbranch_vccnz .LBB0_570

.LBB0_573:
	s_add_i32 s6, s6, 2
	v_pk_add_f32 v[64:65], v[64:65], v[80:81]
	s_add_u32 s90, s90, 0xd0000
	v_pk_add_f32 v[64:65], v[66:67], v[64:65]
	s_addc_u32 s91, s91, 0
	v_pk_add_f32 v[64:65], v[82:83], v[64:65]
	s_and_b64 vcc, exec, s[2:3]
	v_pk_add_f32 v[64:65], v[68:69], v[64:65]
	s_waitcnt lgkmcnt(0)
	v_pk_add_f32 v[64:65], v[84:85], v[64:65]
	s_barrier
	v_pk_add_f32 v[64:65], v[70:71], v[64:65]
	s_nop 0
	v_pk_add_f32 v[64:65], v[86:87], v[64:65]
	s_nop 0
	v_pk_add_f32 v[64:65], v[72:73], v[64:65]
	s_nop 0
	v_pk_add_f32 v[64:65], v[88:89], v[64:65]
	s_nop 0
	v_pk_add_f32 v[64:65], v[74:75], v[64:65]
	s_nop 0
	v_pk_add_f32 v[64:65], v[90:91], v[64:65]
	s_nop 0
	v_pk_add_f32 v[64:65], v[76:77], v[64:65]
	s_nop 0
	v_pk_add_f32 v[64:65], v[92:93], v[64:65]
	s_nop 0
	v_pk_add_f32 v[64:65], v[78:79], v[64:65]
	s_nop 0
	v_pk_add_f32 v[64:65], v[94:95], v[64:65]
	s_nop 0
	v_add_f32_e32 v64, v64, v65
	v_add_f32_e32 v66, v215, v64
	s_nop 0
	v_pk_add_f32 v[64:65], v[96:97], v[112:113]
	s_nop 0
	v_pk_add_f32 v[64:65], v[98:99], v[64:65]
	s_nop 0
	v_pk_add_f32 v[64:65], v[114:115], v[64:65]
	s_nop 0
	v_pk_add_f32 v[64:65], v[100:101], v[64:65]
	s_nop 0
	v_pk_add_f32 v[64:65], v[116:117], v[64:65]
	s_nop 0
	v_pk_add_f32 v[64:65], v[102:103], v[64:65]
	s_nop 0
	v_pk_add_f32 v[64:65], v[118:119], v[64:65]
	s_nop 0
	v_pk_add_f32 v[64:65], v[104:105], v[64:65]
	s_nop 0
	v_pk_add_f32 v[64:65], v[120:121], v[64:65]
	s_nop 0
	v_pk_add_f32 v[64:65], v[106:107], v[64:65]
	s_nop 0
	v_pk_add_f32 v[64:65], v[122:123], v[64:65]
	s_nop 0
	v_pk_add_f32 v[64:65], v[108:109], v[64:65]
	s_nop 0
	v_pk_add_f32 v[64:65], v[124:125], v[64:65]
	s_nop 0
	v_pk_add_f32 v[64:65], v[110:111], v[64:65]
	s_nop 0
	v_pk_add_f32 v[64:65], v[126:127], v[64:65]
	s_nop 0
	v_add_f32_e32 v64, v64, v65
	v_add_f32_e32 v215, v66, v64
	s_cbranch_vccnz .LBB0_594

.LBB0_601:
	v_exp_f32_e32 v143, v95
	v_pk_add_f32 v[64:65], v[96:97], v[112:113]
	v_exp_f32_e32 v159, v79
	v_pk_add_f32 v[64:65], v[98:99], v[64:65]
	v_cvt_pk_bf16_f32 v66, v132, v133
	v_pk_add_f32 v[64:65], v[114:115], v[64:65]
	v_cvt_pk_bf16_f32 v67, v134, v135
	v_pk_add_f32 v[64:65], v[100:101], v[64:65]
	v_cvt_pk_bf16_f32 v68, v136, v137
	v_pk_add_f32 v[64:65], v[116:117], v[64:65]
	v_cvt_pk_bf16_f32 v69, v138, v139
	v_pk_add_f32 v[64:65], v[102:103], v[64:65]
	v_cvt_pk_bf16_f32 v70, v140, v141
	v_pk_add_f32 v[64:65], v[118:119], v[64:65]
	v_cvt_pk_bf16_f32 v71, v142, v143
	v_pk_add_f32 v[64:65], v[104:105], v[64:65]
	v_cvt_pk_bf16_f32 v72, v144, v145
	v_pk_add_f32 v[64:65], v[120:121], v[64:65]
	v_cvt_pk_bf16_f32 v73, v146, v147
	v_pk_add_f32 v[64:65], v[106:107], v[64:65]
	v_cvt_pk_bf16_f32 v74, v148, v149
	v_pk_add_f32 v[64:65], v[122:123], v[64:65]
	v_cvt_pk_bf16_f32 v75, v150, v151
	v_pk_add_f32 v[64:65], v[108:109], v[64:65]
	v_cvt_pk_bf16_f32 v76, v152, v153
	v_pk_add_f32 v[64:65], v[124:125], v[64:65]
	v_cvt_pk_bf16_f32 v77, v154, v155
	v_pk_add_f32 v[64:65], v[110:111], v[64:65]
	v_cvt_pk_bf16_f32 v78, v156, v157
	v_pk_add_f32 v[64:65], v[126:127], v[64:65]
	v_cvt_pk_bf16_f32 v79, v158, v159
	v_add_f32_e32 v64, v64, v65
	v_add_f32_e32 v229, v229, v64
	v_permlane32_swap_b32_e32 v68, v70
	v_pk_add_f32 v[64:65], v[128:129], v[144:145]
	v_permlane32_swap_b32_e32 v69, v71
	v_pk_add_f32 v[64:65], v[130:131], v[64:65]
	v_permlane32_swap_b32_e32 v72, v74
	v_pk_add_f32 v[64:65], v[146:147], v[64:65]
	v_permlane32_swap_b32_e32 v73, v75
	v_pk_add_f32 v[64:65], v[132:133], v[64:65]
	v_permlane32_swap_b32_e32 v76, v78
	v_pk_add_f32 v[64:65], v[148:149], v[64:65]
	v_permlane32_swap_b32_e32 v77, v79
	v_pk_add_f32 v[64:65], v[134:135], v[64:65]
	s_nop 0
	v_pk_add_f32 v[64:65], v[150:151], v[64:65]
	s_nop 0
	v_pk_add_f32 v[64:65], v[136:137], v[64:65]
	s_nop 0
	v_pk_add_f32 v[64:65], v[152:153], v[64:65]
	s_nop 0
	v_pk_add_f32 v[64:65], v[138:139], v[64:65]
	s_nop 0
	v_pk_add_f32 v[64:65], v[154:155], v[64:65]
	s_nop 0
	v_pk_add_f32 v[64:65], v[140:141], v[64:65]
	s_nop 0
	v_pk_add_f32 v[64:65], v[156:157], v[64:65]
	s_nop 0
	v_pk_add_f32 v[64:65], v[142:143], v[64:65]
	s_nop 0
	v_pk_add_f32 v[64:65], v[158:159], v[64:65]
	s_nop 0
	v_add_f32_e32 v64, v64, v65
	v_add_f32_e32 v160, v160, v64
	v_cvt_pk_bf16_f32 v64, v128, v129
	v_cvt_pk_bf16_f32 v65, v130, v131
	s_nop 0
	v_permlane32_swap_b32_e32 v64, v66
	v_permlane32_swap_b32_e32 v65, v67
	v_lshl_add_u32 v96, s23, 13, v228
	ds_read_b64_tr_b16 v[80:81], v96 offset:0
	ds_read_b64_tr_b16 v[82:83], v96 offset:0x400
	ds_read_b64_tr_b16 v[84:85], v96 offset:0x800
	ds_read_b64_tr_b16 v[86:87], v96 offset:0xc00
	ds_read_b64_tr_b16 v[88:89], v96 offset:0x1000
	ds_read_b64_tr_b16 v[90:91], v96 offset:0x1400
	ds_read_b64_tr_b16 v[92:93], v96 offset:0x1800
	ds_read_b64_tr_b16 v[94:95], v96 offset:0x1c00
	s_waitcnt lgkmcnt(0)
	s_nop 0
	v_mfma_f32_32x32x16_bf16 v[48:63], v[210:213], v[80:83], v[48:63]
	v_mfma_f32_32x32x16_bf16 v[0:15], v[64:67], v[80:83], v[0:15]
	ds_read_b64_tr_b16 v[80:81], v96 offset:0x200
	ds_read_b64_tr_b16 v[82:83], v96 offset:0x600
	v_mfma_f32_32x32x16_bf16 v[48:63], v[218:221], v[84:87], v[48:63]
	v_mfma_f32_32x32x16_bf16 v[0:15], v[68:71], v[84:87], v[0:15]
	ds_read_b64_tr_b16 v[84:85], v96 offset:0xa00
	ds_read_b64_tr_b16 v[86:87], v96 offset:0xe00
	v_mfma_f32_32x32x16_bf16 v[48:63], v[222:225], v[88:91], v[48:63]
	v_mfma_f32_32x32x16_bf16 v[0:15], v[72:75], v[88:91], v[0:15]
	ds_read_b64_tr_b16 v[88:89], v96 offset:0x1200
	ds_read_b64_tr_b16 v[90:91], v96 offset:0x1600
	v_mfma_f32_32x32x16_bf16 v[48:63], v[214:217], v[92:95], v[48:63]
	v_mfma_f32_32x32x16_bf16 v[0:15], v[76:79], v[92:95], v[0:15]
	ds_read_b64_tr_b16 v[92:93], v96 offset:0x1a00
	ds_read_b64_tr_b16 v[94:95], v96 offset:0x1e00
	s_waitcnt lgkmcnt(0)
	v_mfma_f32_32x32x16_bf16 v[32:47], v[210:213], v[80:83], v[32:47]
	s_waitcnt vmcnt(0)
	s_add_u32 s74, s74, 0x18000
	s_addc_u32 s75, s75, 0
	s_add_i32 s22, s22, 1
	v_lshl_add_u64 v[236:237], v[236:237], 0, s[20:21]
	s_cmp_eq_u32 s74, 0x300000
	s_waitcnt vmcnt(0)
	v_mfma_f32_32x32x16_bf16 v[16:31], v[64:67], v[80:83], v[16:31]
	s_barrier
	v_mfma_f32_32x32x16_bf16 v[32:47], v[218:221], v[84:87], v[32:47]
	v_mfma_f32_32x32x16_bf16 v[16:31], v[68:71], v[84:87], v[16:31]
	v_mfma_f32_32x32x16_bf16 v[32:47], v[222:225], v[88:91], v[32:47]
	v_mfma_f32_32x32x16_bf16 v[16:31], v[72:75], v[88:91], v[16:31]
	v_mfma_f32_32x32x16_bf16 v[32:47], v[214:217], v[92:95], v[32:47]
	v_mfma_f32_32x32x16_bf16 v[16:31], v[76:79], v[92:95], v[16:31]
	s_cbranch_scc1 .LBB0_622

.LBB0_631:
	v_exp_f32_e32 v143, v95
	v_pk_add_f32 v[64:65], v[96:97], v[112:113]
	v_exp_f32_e32 v159, v79
	v_pk_add_f32 v[64:65], v[98:99], v[64:65]
	v_cvt_pk_bf16_f32 v66, v132, v133
	v_pk_add_f32 v[64:65], v[114:115], v[64:65]
	v_cvt_pk_bf16_f32 v67, v134, v135
	v_pk_add_f32 v[64:65], v[100:101], v[64:65]
	v_cvt_pk_bf16_f32 v68, v136, v137
	v_pk_add_f32 v[64:65], v[116:117], v[64:65]
	v_cvt_pk_bf16_f32 v69, v138, v139
	v_pk_add_f32 v[64:65], v[102:103], v[64:65]
	v_cvt_pk_bf16_f32 v70, v140, v141
	v_pk_add_f32 v[64:65], v[118:119], v[64:65]
	v_cvt_pk_bf16_f32 v71, v142, v143
	v_pk_add_f32 v[64:65], v[104:105], v[64:65]
	v_cvt_pk_bf16_f32 v72, v144, v145
	v_pk_add_f32 v[64:65], v[120:121], v[64:65]
	v_cvt_pk_bf16_f32 v73, v146, v147
	v_pk_add_f32 v[64:65], v[106:107], v[64:65]
	v_cvt_pk_bf16_f32 v74, v148, v149
	v_pk_add_f32 v[64:65], v[122:123], v[64:65]
	v_cvt_pk_bf16_f32 v75, v150, v151
	v_pk_add_f32 v[64:65], v[108:109], v[64:65]
	v_cvt_pk_bf16_f32 v76, v152, v153
	v_pk_add_f32 v[64:65], v[124:125], v[64:65]
	v_cvt_pk_bf16_f32 v77, v154, v155
	v_pk_add_f32 v[64:65], v[110:111], v[64:65]
	v_cvt_pk_bf16_f32 v78, v156, v157
	v_pk_add_f32 v[64:65], v[126:127], v[64:65]
	v_cvt_pk_bf16_f32 v79, v158, v159
	v_add_f32_e32 v64, v64, v65
	v_add_f32_e32 v227, v227, v64
	v_permlane32_swap_b32_e32 v68, v70
	v_pk_add_f32 v[64:65], v[128:129], v[144:145]
	v_permlane32_swap_b32_e32 v69, v71
	v_pk_add_f32 v[64:65], v[130:131], v[64:65]
	v_permlane32_swap_b32_e32 v72, v74
	v_pk_add_f32 v[64:65], v[146:147], v[64:65]
	v_permlane32_swap_b32_e32 v73, v75
	v_pk_add_f32 v[64:65], v[132:133], v[64:65]
	v_permlane32_swap_b32_e32 v76, v78
	v_pk_add_f32 v[64:65], v[148:149], v[64:65]
	v_permlane32_swap_b32_e32 v77, v79
	v_pk_add_f32 v[64:65], v[134:135], v[64:65]
	s_nop 0
	v_pk_add_f32 v[64:65], v[150:151], v[64:65]
	s_nop 0
	v_pk_add_f32 v[64:65], v[136:137], v[64:65]
	s_nop 0
	v_pk_add_f32 v[64:65], v[152:153], v[64:65]
	s_nop 0
	v_pk_add_f32 v[64:65], v[138:139], v[64:65]
	s_nop 0
	v_pk_add_f32 v[64:65], v[154:155], v[64:65]
	s_nop 0
	v_pk_add_f32 v[64:65], v[140:141], v[64:65]
	s_nop 0
	v_pk_add_f32 v[64:65], v[156:157], v[64:65]
	s_nop 0
	v_pk_add_f32 v[64:65], v[142:143], v[64:65]
	s_nop 0
	v_pk_add_f32 v[64:65], v[158:159], v[64:65]
	s_nop 0
	v_add_f32_e32 v64, v64, v65
	v_add_f32_e32 v160, v160, v64
	v_cvt_pk_bf16_f32 v64, v128, v129
	v_cvt_pk_bf16_f32 v65, v130, v131
	s_nop 0
	v_permlane32_swap_b32_e32 v64, v66
	v_permlane32_swap_b32_e32 v65, v67
	v_lshl_add_u32 v96, s33, 13, v226
	ds_read_b64_tr_b16 v[80:81], v96 offset:0
	ds_read_b64_tr_b16 v[82:83], v96 offset:0x400
	ds_read_b64_tr_b16 v[84:85], v96 offset:0x800
	ds_read_b64_tr_b16 v[86:87], v96 offset:0xc00
	ds_read_b64_tr_b16 v[88:89], v96 offset:0x1000
	ds_read_b64_tr_b16 v[90:91], v96 offset:0x1400
	ds_read_b64_tr_b16 v[92:93], v96 offset:0x1800
	ds_read_b64_tr_b16 v[94:95], v96 offset:0x1c00
	s_waitcnt lgkmcnt(0)
	s_nop 0
	v_mfma_f32_32x32x16_bf16 v[48:63], v[194:197], v[80:83], v[48:63]
	v_mfma_f32_32x32x16_bf16 v[0:15], v[64:67], v[80:83], v[0:15]
	ds_read_b64_tr_b16 v[80:81], v96 offset:0x200
	ds_read_b64_tr_b16 v[82:83], v96 offset:0x600
	v_mfma_f32_32x32x16_bf16 v[48:63], v[198:201], v[84:87], v[48:63]
	v_mfma_f32_32x32x16_bf16 v[0:15], v[68:71], v[84:87], v[0:15]
	ds_read_b64_tr_b16 v[84:85], v96 offset:0xa00
	ds_read_b64_tr_b16 v[86:87], v96 offset:0xe00
	v_mfma_f32_32x32x16_bf16 v[48:63], v[202:205], v[88:91], v[48:63]
	v_mfma_f32_32x32x16_bf16 v[0:15], v[72:75], v[88:91], v[0:15]
	ds_read_b64_tr_b16 v[88:89], v96 offset:0x1200
	ds_read_b64_tr_b16 v[90:91], v96 offset:0x1600
	v_mfma_f32_32x32x16_bf16 v[48:63], v[206:209], v[92:95], v[48:63]
	v_mfma_f32_32x32x16_bf16 v[0:15], v[76:79], v[92:95], v[0:15]
	ds_read_b64_tr_b16 v[92:93], v96 offset:0x1a00
	ds_read_b64_tr_b16 v[94:95], v96 offset:0x1e00
	s_waitcnt lgkmcnt(0)
	v_mfma_f32_32x32x16_bf16 v[32:47], v[194:197], v[80:83], v[32:47]
	s_waitcnt vmcnt(0)
	s_add_u32 s90, s90, 0x68000
	s_addc_u32 s91, s91, 0
	s_add_i32 s31, s31, 1
	s_cmp_eq_u32 s90, 0xd00000
	s_waitcnt vmcnt(0)
	s_barrier
	v_mfma_f32_32x32x16_bf16 v[16:31], v[64:67], v[80:83], v[16:31]
	v_mfma_f32_32x32x16_bf16 v[32:47], v[198:201], v[84:87], v[32:47]
	v_mfma_f32_32x32x16_bf16 v[16:31], v[68:71], v[84:87], v[16:31]
	v_mfma_f32_32x32x16_bf16 v[32:47], v[202:205], v[88:91], v[32:47]
	v_mfma_f32_32x32x16_bf16 v[16:31], v[72:75], v[88:91], v[16:31]
	v_mfma_f32_32x32x16_bf16 v[32:47], v[206:209], v[92:95], v[32:47]
	v_mfma_f32_32x32x16_bf16 v[16:31], v[76:79], v[92:95], v[16:31]
	s_cbranch_scc1 .LBB0_652

.LBB0_660:
	s_xor_b64 s[10:11], s[48:49], -1
	v_pk_add_f32 v[64:65], v[64:65], v[80:81]
	s_mov_b64 s[2:3], 0x30000
	v_pk_add_f32 v[64:65], v[66:67], v[64:65]
	s_mov_b64 s[48:49], 0
	v_pk_add_f32 v[64:65], v[82:83], v[64:65]
	s_and_b64 vcc, exec, s[10:11]
	v_pk_add_f32 v[64:65], v[68:69], v[64:65]
	s_waitcnt lgkmcnt(0)
	v_pk_add_f32 v[64:65], v[84:85], v[64:65]
	s_barrier
	v_pk_add_f32 v[64:65], v[70:71], v[64:65]
	s_nop 0
	v_pk_add_f32 v[64:65], v[86:87], v[64:65]
	s_nop 0
	v_pk_add_f32 v[64:65], v[72:73], v[64:65]
	s_nop 0
	v_pk_add_f32 v[64:65], v[88:89], v[64:65]
	s_nop 0
	v_pk_add_f32 v[64:65], v[74:75], v[64:65]
	s_nop 0
	v_pk_add_f32 v[64:65], v[90:91], v[64:65]
	s_nop 0
	v_pk_add_f32 v[64:65], v[76:77], v[64:65]
	s_nop 0
	v_pk_add_f32 v[64:65], v[92:93], v[64:65]
	s_nop 0
	v_pk_add_f32 v[64:65], v[78:79], v[64:65]
	s_nop 0
	v_pk_add_f32 v[64:65], v[94:95], v[64:65]
	s_nop 0
	v_add_f32_e32 v64, v64, v65
	v_add_f32_e32 v66, v211, v64
	s_nop 0
	v_pk_add_f32 v[64:65], v[96:97], v[144:145]
	s_nop 0
	v_pk_add_f32 v[64:65], v[98:99], v[64:65]
	s_nop 0
	v_pk_add_f32 v[64:65], v[146:147], v[64:65]
	s_nop 0
	v_pk_add_f32 v[64:65], v[100:101], v[64:65]
	s_nop 0
	v_pk_add_f32 v[64:65], v[148:149], v[64:65]
	s_nop 0
	v_pk_add_f32 v[64:65], v[102:103], v[64:65]
	s_nop 0
	v_pk_add_f32 v[64:65], v[150:151], v[64:65]
	s_nop 0
	v_pk_add_f32 v[64:65], v[104:105], v[64:65]
	s_nop 0
	v_pk_add_f32 v[64:65], v[152:153], v[64:65]
	s_nop 0
	v_pk_add_f32 v[64:65], v[106:107], v[64:65]
	s_nop 0
	v_pk_add_f32 v[64:65], v[154:155], v[64:65]
	s_nop 0
	v_pk_add_f32 v[64:65], v[108:109], v[64:65]
	s_nop 0
	v_pk_add_f32 v[64:65], v[156:157], v[64:65]
	s_nop 0
	v_pk_add_f32 v[64:65], v[110:111], v[64:65]
	s_nop 0
	v_pk_add_f32 v[64:65], v[158:159], v[64:65]
	s_nop 0
	v_add_f32_e32 v64, v64, v65
	v_add_f32_e32 v211, v66, v64
	s_cbranch_vccnz .LBB0_683

.LBB0_686:
	s_xor_b64 s[22:23], s[48:49], -1
	v_pk_add_f32 v[64:65], v[64:65], v[80:81]
	s_mov_b64 s[2:3], 0x30000
	v_pk_add_f32 v[64:65], v[66:67], v[64:65]
	s_mov_b64 s[48:49], 0
	v_pk_add_f32 v[64:65], v[82:83], v[64:65]
	s_and_b64 vcc, exec, s[22:23]
	v_pk_add_f32 v[64:65], v[68:69], v[64:65]
	s_waitcnt lgkmcnt(0)
	v_pk_add_f32 v[64:65], v[84:85], v[64:65]
	s_barrier
	v_pk_add_f32 v[64:65], v[70:71], v[64:65]
	s_nop 0
	v_pk_add_f32 v[64:65], v[86:87], v[64:65]
	s_nop 0
	v_pk_add_f32 v[64:65], v[72:73], v[64:65]
	s_nop 0
	v_pk_add_f32 v[64:65], v[88:89], v[64:65]
	s_nop 0
	v_pk_add_f32 v[64:65], v[74:75], v[64:65]
	s_nop 0
	v_pk_add_f32 v[64:65], v[90:91], v[64:65]
	s_nop 0
	v_pk_add_f32 v[64:65], v[76:77], v[64:65]
	s_nop 0
	v_pk_add_f32 v[64:65], v[92:93], v[64:65]
	s_nop 0
	v_pk_add_f32 v[64:65], v[78:79], v[64:65]
	s_nop 0
	v_pk_add_f32 v[64:65], v[94:95], v[64:65]
	s_nop 0
	v_add_f32_e32 v64, v64, v65
	v_add_f32_e32 v66, v211, v64
	s_nop 0
	v_pk_add_f32 v[64:65], v[96:97], v[112:113]
	s_nop 0
	v_pk_add_f32 v[64:65], v[98:99], v[64:65]
	s_nop 0
	v_pk_add_f32 v[64:65], v[114:115], v[64:65]
	s_nop 0
	v_pk_add_f32 v[64:65], v[100:101], v[64:65]
	s_nop 0
	v_pk_add_f32 v[64:65], v[116:117], v[64:65]
	s_nop 0
	v_pk_add_f32 v[64:65], v[102:103], v[64:65]
	s_nop 0
	v_pk_add_f32 v[64:65], v[118:119], v[64:65]
	s_nop 0
	v_pk_add_f32 v[64:65], v[104:105], v[64:65]
	s_nop 0
	v_pk_add_f32 v[64:65], v[120:121], v[64:65]
	s_nop 0
	v_pk_add_f32 v[64:65], v[106:107], v[64:65]
	s_nop 0
	v_pk_add_f32 v[64:65], v[122:123], v[64:65]
	s_nop 0
	v_pk_add_f32 v[64:65], v[108:109], v[64:65]
	s_nop 0
	v_pk_add_f32 v[64:65], v[124:125], v[64:65]
	s_nop 0
	v_pk_add_f32 v[64:65], v[110:111], v[64:65]
	s_nop 0
	v_pk_add_f32 v[64:65], v[126:127], v[64:65]
	s_nop 0
	v_add_f32_e32 v64, v64, v65
	v_add_f32_e32 v211, v66, v64
	s_cbranch_vccnz .LBB0_707
